# baseline (speedup 1.0000x reference)
.LBB2_57:
	v_readlane_b32 s44, v252, 28
	v_readlane_b32 s45, v252, 29
	s_andn2_b64 vcc, exec, s[44:45]
	v_readlane_b32 s48, v252, 33
	v_readlane_b32 s49, v252, 34
	v_readlane_b32 s50, v252, 35
	s_waitcnt lgkmcnt(0)
	s_barrier
	s_cbranch_vccnz .LBB2_1
	ds_read2st64_b32 v[4:5], v207 offset0:128 offset1:132
	v_max_f32_e32 v2, v232, v232
	ds_read2st64_b32 v[44:45], v207 offset0:64 offset1:68
	s_waitcnt lgkmcnt(1)
	v_max_f32_e32 v38, v4, v4
	v_max_f32_e32 v2, v2, v38
	v_sub_f32_e32 v38, v232, v2
	v_sub_f32_e32 v2, v4, v2
	v_exp_f32_e32 v39, v2
	v_exp_f32_e32 v38, v38
	v_mov_b32_e32 v165, v5
	v_mul_f32_e32 v2, v5, v39
	v_pk_fma_f32 v[4:5], v[164:165], v[38:39], v[2:3] op_sel_hi:[1,1,0]
	s_nop 0
	v_mov_b32_e32 v2, v4
	s_nop 1
	v_permlane32_swap_b32_e32 v4, v2
	v_add_f32_e32 v2, v4, v2
	v_div_scale_f32 v4, s[0:1], v2, v2, 1.0
	v_rcp_f32_e32 v5, v4
	v_div_scale_f32 v40, vcc, 1.0, v2, 1.0
	v_readlane_b32 s0, v252, 37
	v_fma_f32 v41, -v4, v5, 1.0
	v_fmac_f32_e32 v5, v41, v5
	v_mul_f32_e32 v41, v40, v5
	v_fma_f32 v42, -v4, v41, v40
	v_fmac_f32_e32 v41, v42, v5
	v_fma_f32 v4, -v4, v41, v40
	v_div_fmas_f32 v4, v4, v5, v41
	v_div_fixup_f32 v2, v4, v2, 1.0
	v_mul_f32_e32 v4, v38, v2
	v_mul_f32_e32 v38, v39, v2
	v_readfirstlane_b32 s36, v162
	v_readfirstlane_b32 s37, v163
	v_or_b32_e32 v2, s0, v0
	v_and_b32_e32 v40, 31, v0
	v_and_b32_e32 v41, 7, v40
	v_lshrrev_b32_e32 v42, 3, v40
	v_add_u32_e32 v42, v42, v159
	v_and_b32_e32 v43, 0xfffff000, v181
	v_lshl_add_u32 v44, v40, 7, v43
	v_lshl_add_u32 v44, v159, 1, v44
	v_lshlrev_b32_e32 v45, 4, v41
	v_xor_b32_e32 v46, v41, v42
	v_lshlrev_b32_e32 v46, 4, v46
	v_lshl_add_u32 v46, v42, 7, v46
	v_add_u32_e32 v46, v46, v43
	v_and_b32_e32 v2, 0xffffffe0, v2
	v_add_u32_e32 v2, v2, v42
	v_lshlrev_b32_e32 v2, 11, v2
	v_lshl_add_u32 v47, v41, 4, v2
	ds_read2st64_b32 v[86:87], v207 offset1:4
	ds_read2st64_b32 v[88:89], v207 offset0:8 offset1:12
	ds_read2st64_b32 v[90:91], v207 offset0:16 offset1:20
	ds_read2st64_b32 v[92:93], v207 offset0:24 offset1:28
	ds_read2st64_b32 v[94:95], v207 offset0:32 offset1:36
	ds_read2st64_b32 v[96:97], v207 offset0:40 offset1:44
	ds_read2st64_b32 v[98:99], v207 offset0:48 offset1:52
	ds_read2st64_b32 v[100:101], v207 offset0:56 offset1:60
	s_waitcnt lgkmcnt(7)
	v_pk_mul_f32 v[86:87], v[38:39], v[86:87] op_sel_hi:[0,1]
	v_pk_fma_f32 v[22:23], v[4:5], v[22:23], v[86:87] op_sel_hi:[0,1,1]
	s_waitcnt lgkmcnt(6)
	v_pk_mul_f32 v[88:89], v[38:39], v[88:89] op_sel_hi:[0,1]
	v_pk_fma_f32 v[24:25], v[4:5], v[24:25], v[88:89] op_sel_hi:[0,1,1]
	s_waitcnt lgkmcnt(5)
	v_pk_mul_f32 v[90:91], v[38:39], v[90:91] op_sel_hi:[0,1]
	v_pk_fma_f32 v[26:27], v[4:5], v[26:27], v[90:91] op_sel_hi:[0,1,1]
	s_waitcnt lgkmcnt(4)
	v_pk_mul_f32 v[92:93], v[38:39], v[92:93] op_sel_hi:[0,1]
	v_pk_fma_f32 v[28:29], v[4:5], v[28:29], v[92:93] op_sel_hi:[0,1,1]
	s_waitcnt lgkmcnt(3)
	v_pk_mul_f32 v[94:95], v[38:39], v[94:95] op_sel_hi:[0,1]
	v_pk_fma_f32 v[30:31], v[4:5], v[30:31], v[94:95] op_sel_hi:[0,1,1]
	s_waitcnt lgkmcnt(2)
	v_pk_mul_f32 v[96:97], v[38:39], v[96:97] op_sel_hi:[0,1]
	v_pk_fma_f32 v[32:33], v[4:5], v[32:33], v[96:97] op_sel_hi:[0,1,1]
	s_waitcnt lgkmcnt(1)
	v_pk_mul_f32 v[98:99], v[38:39], v[98:99] op_sel_hi:[0,1]
	v_pk_fma_f32 v[34:35], v[4:5], v[34:35], v[98:99] op_sel_hi:[0,1,1]
	s_waitcnt lgkmcnt(0)
	v_pk_mul_f32 v[100:101], v[38:39], v[100:101] op_sel_hi:[0,1]
	v_pk_fma_f32 v[36:37], v[4:5], v[36:37], v[100:101] op_sel_hi:[0,1,1]
	ds_read2st64_b32 v[102:103], v207 offset0:64 offset1:68
	ds_read2st64_b32 v[104:105], v207 offset0:72 offset1:76
	ds_read2st64_b32 v[106:107], v207 offset0:80 offset1:84
	ds_read2st64_b32 v[108:109], v207 offset0:88 offset1:92
	ds_read2st64_b32 v[110:111], v207 offset0:96 offset1:100
	ds_read2st64_b32 v[112:113], v207 offset0:104 offset1:108
	ds_read2st64_b32 v[114:115], v207 offset0:112 offset1:116
	ds_read2st64_b32 v[116:117], v207 offset0:120 offset1:124
	s_waitcnt lgkmcnt(7)
	v_pk_mul_f32 v[102:103], v[38:39], v[102:103] op_sel_hi:[0,1]
	v_pk_fma_f32 v[6:7], v[4:5], v[6:7], v[102:103] op_sel_hi:[0,1,1]
	s_waitcnt lgkmcnt(6)
	v_pk_mul_f32 v[104:105], v[38:39], v[104:105] op_sel_hi:[0,1]
	v_pk_fma_f32 v[8:9], v[4:5], v[8:9], v[104:105] op_sel_hi:[0,1,1]
	s_waitcnt lgkmcnt(5)
	v_pk_mul_f32 v[106:107], v[38:39], v[106:107] op_sel_hi:[0,1]
	v_pk_fma_f32 v[10:11], v[4:5], v[10:11], v[106:107] op_sel_hi:[0,1,1]
	s_waitcnt lgkmcnt(4)
	v_pk_mul_f32 v[108:109], v[38:39], v[108:109] op_sel_hi:[0,1]
	v_pk_fma_f32 v[12:13], v[4:5], v[12:13], v[108:109] op_sel_hi:[0,1,1]
	s_waitcnt lgkmcnt(3)
	v_pk_mul_f32 v[110:111], v[38:39], v[110:111] op_sel_hi:[0,1]
	v_pk_fma_f32 v[14:15], v[4:5], v[14:15], v[110:111] op_sel_hi:[0,1,1]
	s_waitcnt lgkmcnt(2)
	v_pk_mul_f32 v[112:113], v[38:39], v[112:113] op_sel_hi:[0,1]
	v_pk_fma_f32 v[16:17], v[4:5], v[16:17], v[112:113] op_sel_hi:[0,1,1]
	s_waitcnt lgkmcnt(1)
	v_pk_mul_f32 v[114:115], v[38:39], v[114:115] op_sel_hi:[0,1]
	v_pk_fma_f32 v[18:19], v[4:5], v[18:19], v[114:115] op_sel_hi:[0,1,1]
	s_waitcnt lgkmcnt(0)
	v_pk_mul_f32 v[116:117], v[38:39], v[116:117] op_sel_hi:[0,1]
	v_pk_fma_f32 v[20:21], v[4:5], v[20:21], v[116:117] op_sel_hi:[0,1,1]
	v_cvt_pk_f16_f32 v22, v22, v23
	v_cvt_pk_f16_f32 v23, v24, v25
	v_cvt_pk_f16_f32 v24, v26, v27
	v_cvt_pk_f16_f32 v25, v28, v29
	v_cvt_pk_f16_f32 v30, v30, v31
	v_cvt_pk_f16_f32 v31, v32, v33
	v_cvt_pk_f16_f32 v32, v34, v35
	v_cvt_pk_f16_f32 v33, v36, v37
	v_cvt_pk_f16_f32 v6, v6, v7
	v_cvt_pk_f16_f32 v7, v8, v9
	v_cvt_pk_f16_f32 v8, v10, v11
	v_cvt_pk_f16_f32 v9, v12, v13
	v_cvt_pk_f16_f32 v14, v14, v15
	v_cvt_pk_f16_f32 v15, v16, v17
	v_cvt_pk_f16_f32 v16, v18, v19
	v_cvt_pk_f16_f32 v17, v20, v21
	v_add_u32_e32 v48, v44, v45
	ds_write_b64 v48, v[22:23]
	v_xor_b32_e32 v48, 0x10, v45
	v_add_u32_e32 v48, v44, v48
	ds_write_b64 v48, v[24:25]
	v_xor_b32_e32 v48, 0x20, v45
	v_add_u32_e32 v48, v44, v48
	ds_write_b64 v48, v[30:31]
	v_xor_b32_e32 v48, 0x30, v45
	v_add_u32_e32 v48, v44, v48
	ds_write_b64 v48, v[32:33]
	v_xor_b32_e32 v48, 0x40, v45
	v_add_u32_e32 v48, v44, v48
	ds_write_b64 v48, v[6:7]
	v_xor_b32_e32 v48, 0x50, v45
	v_add_u32_e32 v48, v44, v48
	ds_write_b64 v48, v[8:9]
	v_xor_b32_e32 v48, 0x60, v45
	v_add_u32_e32 v48, v44, v48
	ds_write_b64 v48, v[14:15]
	v_xor_b32_e32 v48, 0x70, v45
	v_add_u32_e32 v48, v44, v48
	ds_write_b64 v48, v[16:17]
	ds_read_b128 v[86:89], v46
	ds_read_b128 v[90:93], v46 offset:1024
	ds_read_b128 v[94:97], v46 offset:2048
	ds_read_b128 v[98:101], v46 offset:3072
	s_waitcnt lgkmcnt(3)
	global_store_dwordx4 v47, v[86:89], s[36:37]
	s_waitcnt lgkmcnt(2)
	v_add_u32_e32 v47, 0x4000, v47
	s_nop 0
	global_store_dwordx4 v47, v[90:93], s[36:37]
	s_waitcnt lgkmcnt(1)
	v_add_u32_e32 v47, 0x4000, v47
	s_nop 0
	global_store_dwordx4 v47, v[94:97], s[36:37]
	s_waitcnt lgkmcnt(0)
	v_add_u32_e32 v47, 0x4000, v47
	s_nop 0
	global_store_dwordx4 v47, v[98:101], s[36:37]
	s_branch .LBB2_1
